# int8 expert-weight conversion loop: the four per-row scale loads issued with the item's 16 weight loads, vmcnt(0) drains (which also waited for the previous row's store) removed
# speedup vs baseline: 1.0084x; 1.0027x over previous
.LBB0_871:
	s_or_b64 exec, exec, s[4:5]
	v_mov_b32_e32 v181, s17
	v_lshlrev_b32_e32 v181, 6, v181
	v_and_b32_e32 v181, 0xffffff00, v181
	v_or_b32_e32 v180, s18, v71
	v_and_b32_e32 v180, 0x67, v180
	v_or_b32_e32 v180, v181, v180
	v_or_b32_e32 v182, 0x80, v180
	v_cndmask_b32_e64 v182, v180, v182, s[6:7]
	v_ashrrev_i32_e32 v183, 31, v182
	v_lshl_add_u64 v[184:185], v[182:183], 2, s[0:1]
	global_load_dword v176, v[184:185], off
	v_or_b32_e32 v180, s18, v72
	v_and_b32_e32 v180, 0x6f, v180
	v_or_b32_e32 v180, v181, v180
	v_or_b32_e32 v182, 0x80, v180
	v_cndmask_b32_e64 v182, v180, v182, s[6:7]
	v_ashrrev_i32_e32 v183, 31, v182
	v_lshl_add_u64 v[184:185], v[182:183], 2, s[0:1]
	global_load_dword v177, v[184:185], off
	v_or_b32_e32 v180, s18, v73
	v_and_b32_e32 v180, 0x77, v180
	v_or_b32_e32 v180, v181, v180
	v_or_b32_e32 v182, 0x80, v180
	v_cndmask_b32_e64 v182, v180, v182, s[6:7]
	v_ashrrev_i32_e32 v183, 31, v182
	v_lshl_add_u64 v[184:185], v[182:183], 2, s[0:1]
	global_load_dword v178, v[184:185], off
	v_or_b32_e32 v180, s18, v74
	v_and_b32_e32 v180, 0x7f, v180
	v_or_b32_e32 v180, v181, v180
	v_or_b32_e32 v182, 0x80, v180
	v_cndmask_b32_e64 v182, v180, v182, s[6:7]
	v_ashrrev_i32_e32 v183, 31, v182
	v_lshl_add_u64 v[184:185], v[182:183], 2, s[0:1]
	global_load_dword v179, v[184:185], off
	s_waitcnt vmcnt(0)
	ds_write2_b32 v76, v2, v3 offset1:1
	ds_write2_b32 v76, v4, v5 offset0:2 offset1:3
	v_add_u32_e32 v2, 0x420, v76
	ds_write2_b32 v2, v10, v11 offset1:1
	v_add_u32_e32 v2, 0x428, v76
	ds_write2_b32 v2, v12, v13 offset1:1
	v_add_u32_e32 v2, 0x840, v76
	ds_write2_b32 v2, v6, v7 offset1:1
	v_add_u32_e32 v2, 0x848, v76
	ds_write2_b32 v2, v8, v9 offset1:1
	v_add_u32_e32 v2, 0xc60, v76
	ds_write2_b32 v2, v18, v19 offset1:1
	v_add_u32_e32 v2, 0xc68, v76
	ds_write2_b32 v2, v20, v21 offset1:1
	v_add_u32_e32 v2, 0x1080, v76
	ds_write2_b32 v2, v14, v15 offset1:1
	v_add_u32_e32 v2, 0x1088, v76
	ds_write2_b32 v2, v16, v17 offset1:1
	v_add_u32_e32 v2, 0x14a0, v76
	ds_write2_b32 v2, v26, v27 offset1:1
	v_add_u32_e32 v2, 0x14a8, v76
	ds_write2_b32 v2, v28, v29 offset1:1
	v_add_u32_e32 v2, 0x18c0, v76
	ds_write2_b32 v2, v22, v23 offset1:1
	v_add_u32_e32 v2, 0x18c8, v76
	ds_write2_b32 v2, v24, v25 offset1:1
	v_add_u32_e32 v2, 0x1ce0, v76
	ds_write2_b32 v2, v34, v35 offset1:1
	v_add_u32_e32 v2, 0x1ce8, v76
	ds_write2_b32 v2, v36, v37 offset1:1
	v_add_u32_e32 v2, 0x2100, v76
	ds_write2_b32 v2, v30, v31 offset1:1
	v_add_u32_e32 v2, 0x2108, v76
	ds_write2_b32 v2, v32, v33 offset1:1
	v_add_u32_e32 v2, 0x2520, v76
	ds_write2_b32 v2, v42, v43 offset1:1
	v_add_u32_e32 v2, 0x2528, v76
	ds_write2_b32 v2, v44, v45 offset1:1
	v_add_u32_e32 v2, 0x2940, v76
	ds_write2_b32 v2, v38, v39 offset1:1
	v_add_u32_e32 v2, 0x2948, v76
	ds_write2_b32 v2, v40, v41 offset1:1
	v_add_u32_e32 v2, 0x2d60, v76
	ds_write2_b32 v2, v50, v51 offset1:1
	v_add_u32_e32 v2, 0x2d68, v76
	ds_write2_b32 v2, v52, v53 offset1:1
	v_add_u32_e32 v2, 0x3180, v76
	ds_write2_b32 v2, v46, v47 offset1:1
	v_add_u32_e32 v2, 0x3188, v76
	ds_write2_b32 v2, v48, v49 offset1:1
	v_add_u32_e32 v2, 0x35a0, v76
	ds_write2_b32 v2, v58, v59 offset1:1
	v_add_u32_e32 v2, 0x35a8, v76
	ds_write2_b32 v2, v60, v61 offset1:1
	v_add_u32_e32 v2, 0x39c0, v76
	ds_write2_b32 v2, v54, v55 offset1:1
	v_add_u32_e32 v2, 0x39c8, v76
	ds_write2_b32 v2, v56, v57 offset1:1
	v_add_u32_e32 v2, 0x3de0, v76
	ds_write2_b32 v2, v62, v63 offset1:1
	v_add_u32_e32 v2, 0x3de8, v76
	ds_write2_b32 v2, v64, v65 offset1:1
	s_waitcnt lgkmcnt(0)
	s_ashr_i32 s3, s2, 31
	v_or_b32_e32 v5, s18, v71
	v_lshl_add_u64 v[2:3], v[66:67], 0, s[2:3]
	v_cmp_gt_i32_e32 vcc, s15, v5
	v_add_u32_e32 v4, 0x400, v75
	s_and_saveexec_b64 s[2:3], vcc
	s_cbranch_execz .LBB0_873
	s_lshl_b32 s4, s17, 6
	s_and_b32 s4, s4, 0xffffff00
	v_and_b32_e32 v5, 0x67, v5
	v_or_b32_e32 v5, s4, v5
	v_or_b32_e32 v6, 0x80, v5
	v_cndmask_b32_e64 v6, v5, v6, s[6:7]
	v_ashrrev_i32_e32 v7, 31, v6
	v_lshl_add_u64 v[8:9], v[6:7], 2, s[0:1]
	v_mov_b32_e32 v5, v176
	v_lshlrev_b64 v[24:25], 11, v[6:7]
	ds_read2_b32 v[8:9], v75 offset1:33
	ds_read2_b32 v[10:11], v75 offset0:66 offset1:99
	ds_read2_b32 v[12:13], v75 offset0:132 offset1:165
	ds_read2_b32 v[14:15], v75 offset0:198 offset1:231
	ds_read2_b32 v[16:17], v4 offset0:8 offset1:41
	ds_read2_b32 v[18:19], v4 offset0:74 offset1:107
	ds_read2_b32 v[20:21], v4 offset0:140 offset1:173
	ds_read2_b32 v[22:23], v4 offset0:206 offset1:239
	s_nop 0
	v_div_scale_f32 v26, s[4:5], v5, v5, 1.0
	v_rcp_f32_e32 v27, v26
	v_div_scale_f32 v6, vcc, 1.0, v5, 1.0
	v_fma_f32 v7, -v26, v27, 1.0
	v_fmac_f32_e32 v27, v7, v27
	v_mul_f32_e32 v7, v6, v27
	v_fma_f32 v28, -v26, v7, v6
	v_fmac_f32_e32 v7, v28, v27
	v_fma_f32 v6, -v26, v7, v6
	v_div_fmas_f32 v6, v6, v27, v7
	v_div_fixup_f32 v5, v6, v5, 1.0
	s_waitcnt lgkmcnt(7)
	v_fmaak_f32 v6, v8, v5, 0x43000000
	s_waitcnt lgkmcnt(6)
	v_fmaak_f32 v8, v5, v10, 0x43000000
	s_waitcnt lgkmcnt(5)
	v_fmaak_f32 v10, v5, v12, 0x43000000
	s_waitcnt lgkmcnt(4)
	v_fmaak_f32 v12, v5, v14, 0x43000000
	s_waitcnt lgkmcnt(3)
	v_fmaak_f32 v14, v5, v16, 0x43000000
	s_waitcnt lgkmcnt(2)
	v_fmaak_f32 v16, v5, v18, 0x43000000
	s_waitcnt lgkmcnt(1)
	v_fmaak_f32 v18, v5, v20, 0x43000000
	v_fmaak_f32 v7, v5, v9, 0x43000000
	v_fmaak_f32 v9, v5, v11, 0x43000000
	v_fmaak_f32 v11, v5, v13, 0x43000000
	v_fmaak_f32 v13, v5, v15, 0x43000000
	v_fmaak_f32 v15, v5, v17, 0x43000000
	v_fmaak_f32 v17, v5, v19, 0x43000000
	v_fmaak_f32 v19, v5, v21, 0x43000000
	v_rndne_f32_e32 v6, v6
	v_rndne_f32_e32 v10, v10
	v_rndne_f32_e32 v14, v14
	v_rndne_f32_e32 v18, v18
	s_waitcnt lgkmcnt(0)
	v_fmaak_f32 v20, v5, v22, 0x43000000
	v_rndne_f32_e32 v7, v7
	v_rndne_f32_e32 v11, v11
	v_rndne_f32_e32 v15, v15
	v_rndne_f32_e32 v19, v19
	v_cvt_pk_u8_f32 v6, v6, 0, 0
	v_cvt_pk_u8_f32 v10, v10, 0, 0
	v_cvt_pk_u8_f32 v14, v14, 0, 0
	v_cvt_pk_u8_f32 v18, v18, 0, 0
	v_fmaak_f32 v5, v5, v23, 0x43000000
	v_rndne_f32_e32 v8, v8
	v_rndne_f32_e32 v12, v12
	v_rndne_f32_e32 v16, v16
	v_rndne_f32_e32 v20, v20
	v_cvt_pk_u8_f32 v6, v7, 1, v6
	v_cvt_pk_u8_f32 v7, v11, 1, v10
	v_cvt_pk_u8_f32 v10, v15, 1, v14
	v_cvt_pk_u8_f32 v11, v19, 1, v18
	v_rndne_f32_e32 v9, v9
	v_rndne_f32_e32 v13, v13
	v_rndne_f32_e32 v17, v17
	v_rndne_f32_e32 v5, v5
	v_cvt_pk_u8_f32 v6, v8, 2, v6
	v_cvt_pk_u8_f32 v7, v12, 2, v7
	v_cvt_pk_u8_f32 v8, v16, 2, v10
	v_cvt_pk_u8_f32 v10, v20, 2, v11
	v_cvt_pk_u8_f32 v6, v9, 3, v6
	v_cvt_pk_u8_f32 v7, v13, 3, v7
	v_cvt_pk_u8_f32 v8, v17, 3, v8
	v_cvt_pk_u8_f32 v5, v5, 3, v10
	v_xor_b32_e32 v6, 0x80808080, v6
	v_xor_b32_e32 v7, 0x80808080, v7
	v_xor_b32_e32 v8, 0x80808080, v8
	v_xor_b32_e32 v9, 0x80808080, v5
	v_lshl_add_u64 v[10:11], v[2:3], 0, v[24:25]
	global_store_dwordx4 v[10:11], v[6:9], off nt
.LBB0_873:
	s_or_b64 exec, exec, s[2:3]
	v_or_b32_e32 v5, s18, v72
	v_cmp_gt_i32_e32 vcc, s15, v5
	s_and_saveexec_b64 s[2:3], vcc
	s_cbranch_execz .LBB0_875
	s_lshl_b32 s4, s17, 6
	s_and_b32 s4, s4, 0xffffff00
	v_and_b32_e32 v5, 0x6f, v5
	v_or_b32_e32 v5, s4, v5
	v_or_b32_e32 v6, 0x80, v5
	v_cndmask_b32_e64 v6, v5, v6, s[6:7]
	v_ashrrev_i32_e32 v7, 31, v6
	v_lshl_add_u64 v[8:9], v[6:7], 2, s[0:1]
	v_mov_b32_e32 v5, v177
	v_lshlrev_b64 v[24:25], 11, v[6:7]
	ds_read2_b32 v[8:9], v75 offset0:8 offset1:41
	ds_read2_b32 v[10:11], v75 offset0:74 offset1:107
	ds_read2_b32 v[12:13], v75 offset0:140 offset1:173
	ds_read2_b32 v[14:15], v75 offset0:206 offset1:239
	ds_read2_b32 v[16:17], v4 offset0:16 offset1:49
	ds_read2_b32 v[18:19], v4 offset0:82 offset1:115
	ds_read2_b32 v[20:21], v4 offset0:148 offset1:181
	ds_read2_b32 v[22:23], v4 offset0:214 offset1:247
	s_nop 0
	v_div_scale_f32 v26, s[4:5], v5, v5, 1.0
	v_rcp_f32_e32 v27, v26
	v_div_scale_f32 v6, vcc, 1.0, v5, 1.0
	v_fma_f32 v7, -v26, v27, 1.0
	v_fmac_f32_e32 v27, v7, v27
	v_mul_f32_e32 v7, v6, v27
	v_fma_f32 v28, -v26, v7, v6
	v_fmac_f32_e32 v7, v28, v27
	v_fma_f32 v6, -v26, v7, v6
	v_div_fmas_f32 v6, v6, v27, v7
	v_div_fixup_f32 v5, v6, v5, 1.0
	s_waitcnt lgkmcnt(7)
	v_fmaak_f32 v6, v8, v5, 0x43000000
	s_waitcnt lgkmcnt(6)
	v_fmaak_f32 v8, v5, v10, 0x43000000
	s_waitcnt lgkmcnt(5)
	v_fmaak_f32 v10, v5, v12, 0x43000000
	s_waitcnt lgkmcnt(4)
	v_fmaak_f32 v12, v5, v14, 0x43000000
	s_waitcnt lgkmcnt(3)
	v_fmaak_f32 v14, v5, v16, 0x43000000
	s_waitcnt lgkmcnt(2)
	v_fmaak_f32 v16, v5, v18, 0x43000000
	s_waitcnt lgkmcnt(1)
	v_fmaak_f32 v18, v5, v20, 0x43000000
	v_fmaak_f32 v7, v5, v9, 0x43000000
	v_fmaak_f32 v9, v5, v11, 0x43000000
	v_fmaak_f32 v11, v5, v13, 0x43000000
	v_fmaak_f32 v13, v5, v15, 0x43000000
	v_fmaak_f32 v15, v5, v17, 0x43000000
	v_fmaak_f32 v17, v5, v19, 0x43000000
	v_fmaak_f32 v19, v5, v21, 0x43000000
	v_rndne_f32_e32 v6, v6
	v_rndne_f32_e32 v10, v10
	v_rndne_f32_e32 v14, v14
	v_rndne_f32_e32 v18, v18
	s_waitcnt lgkmcnt(0)
	v_fmaak_f32 v20, v5, v22, 0x43000000
	v_rndne_f32_e32 v7, v7
	v_rndne_f32_e32 v11, v11
	v_rndne_f32_e32 v15, v15
	v_rndne_f32_e32 v19, v19
	v_cvt_pk_u8_f32 v6, v6, 0, 0
	v_cvt_pk_u8_f32 v10, v10, 0, 0
	v_cvt_pk_u8_f32 v14, v14, 0, 0
	v_cvt_pk_u8_f32 v18, v18, 0, 0
	v_fmaak_f32 v5, v5, v23, 0x43000000
	v_rndne_f32_e32 v8, v8
	v_rndne_f32_e32 v12, v12
	v_rndne_f32_e32 v16, v16
	v_rndne_f32_e32 v20, v20
	v_cvt_pk_u8_f32 v6, v7, 1, v6
	v_cvt_pk_u8_f32 v7, v11, 1, v10
	v_cvt_pk_u8_f32 v10, v15, 1, v14
	v_cvt_pk_u8_f32 v11, v19, 1, v18
	v_rndne_f32_e32 v9, v9
	v_rndne_f32_e32 v13, v13
	v_rndne_f32_e32 v17, v17
	v_rndne_f32_e32 v5, v5
	v_cvt_pk_u8_f32 v6, v8, 2, v6
	v_cvt_pk_u8_f32 v7, v12, 2, v7
	v_cvt_pk_u8_f32 v8, v16, 2, v10
	v_cvt_pk_u8_f32 v10, v20, 2, v11
	v_cvt_pk_u8_f32 v6, v9, 3, v6
	v_cvt_pk_u8_f32 v7, v13, 3, v7
	v_cvt_pk_u8_f32 v8, v17, 3, v8
	v_cvt_pk_u8_f32 v5, v5, 3, v10
	v_xor_b32_e32 v6, 0x80808080, v6
	v_xor_b32_e32 v7, 0x80808080, v7
	v_xor_b32_e32 v8, 0x80808080, v8
	v_xor_b32_e32 v9, 0x80808080, v5
	v_lshl_add_u64 v[10:11], v[2:3], 0, v[24:25]
	global_store_dwordx4 v[10:11], v[6:9], off nt
.LBB0_875:
	s_or_b64 exec, exec, s[2:3]
	v_or_b32_e32 v5, s18, v73
	v_cmp_gt_i32_e32 vcc, s15, v5
	s_and_saveexec_b64 s[2:3], vcc
	s_cbranch_execz .LBB0_877
	s_lshl_b32 s4, s17, 6
	s_and_b32 s4, s4, 0xffffff00
	v_and_b32_e32 v5, 0x77, v5
	v_or_b32_e32 v5, s4, v5
	v_or_b32_e32 v6, 0x80, v5
	v_cndmask_b32_e64 v6, v5, v6, s[6:7]
	v_ashrrev_i32_e32 v7, 31, v6
	v_lshl_add_u64 v[8:9], v[6:7], 2, s[0:1]
	v_mov_b32_e32 v5, v178
	v_lshlrev_b64 v[24:25], 11, v[6:7]
	ds_read2_b32 v[8:9], v75 offset0:16 offset1:49
	ds_read2_b32 v[10:11], v75 offset0:82 offset1:115
	ds_read2_b32 v[12:13], v75 offset0:148 offset1:181
	ds_read2_b32 v[14:15], v75 offset0:214 offset1:247
	ds_read2_b32 v[16:17], v4 offset0:24 offset1:57
	ds_read2_b32 v[18:19], v4 offset0:90 offset1:123
	ds_read2_b32 v[20:21], v4 offset0:156 offset1:189
	ds_read2_b32 v[22:23], v4 offset0:222 offset1:255
	s_nop 0
	v_div_scale_f32 v26, s[4:5], v5, v5, 1.0
	v_rcp_f32_e32 v27, v26
	v_div_scale_f32 v6, vcc, 1.0, v5, 1.0
	v_fma_f32 v7, -v26, v27, 1.0
	v_fmac_f32_e32 v27, v7, v27
	v_mul_f32_e32 v7, v6, v27
	v_fma_f32 v28, -v26, v7, v6
	v_fmac_f32_e32 v7, v28, v27
	v_fma_f32 v6, -v26, v7, v6
	v_div_fmas_f32 v6, v6, v27, v7
	v_div_fixup_f32 v5, v6, v5, 1.0
	s_waitcnt lgkmcnt(7)
	v_fmaak_f32 v6, v8, v5, 0x43000000
	s_waitcnt lgkmcnt(6)
	v_fmaak_f32 v8, v5, v10, 0x43000000
	s_waitcnt lgkmcnt(5)
	v_fmaak_f32 v10, v5, v12, 0x43000000
	s_waitcnt lgkmcnt(4)
	v_fmaak_f32 v12, v5, v14, 0x43000000
	s_waitcnt lgkmcnt(3)
	v_fmaak_f32 v14, v5, v16, 0x43000000
	s_waitcnt lgkmcnt(2)
	v_fmaak_f32 v16, v5, v18, 0x43000000
	s_waitcnt lgkmcnt(1)
	v_fmaak_f32 v18, v5, v20, 0x43000000
	v_fmaak_f32 v7, v5, v9, 0x43000000
	v_fmaak_f32 v9, v5, v11, 0x43000000
	v_fmaak_f32 v11, v5, v13, 0x43000000
	v_fmaak_f32 v13, v5, v15, 0x43000000
	v_fmaak_f32 v15, v5, v17, 0x43000000
	v_fmaak_f32 v17, v5, v19, 0x43000000
	v_fmaak_f32 v19, v5, v21, 0x43000000
	v_rndne_f32_e32 v6, v6
	v_rndne_f32_e32 v10, v10
	v_rndne_f32_e32 v14, v14
	v_rndne_f32_e32 v18, v18
	s_waitcnt lgkmcnt(0)
	v_fmaak_f32 v20, v5, v22, 0x43000000
	v_rndne_f32_e32 v7, v7
	v_rndne_f32_e32 v11, v11
	v_rndne_f32_e32 v15, v15
	v_rndne_f32_e32 v19, v19
	v_cvt_pk_u8_f32 v6, v6, 0, 0
	v_cvt_pk_u8_f32 v10, v10, 0, 0
	v_cvt_pk_u8_f32 v14, v14, 0, 0
	v_cvt_pk_u8_f32 v18, v18, 0, 0
	v_fmaak_f32 v5, v5, v23, 0x43000000
	v_rndne_f32_e32 v8, v8
	v_rndne_f32_e32 v12, v12
	v_rndne_f32_e32 v16, v16
	v_rndne_f32_e32 v20, v20
	v_cvt_pk_u8_f32 v6, v7, 1, v6
	v_cvt_pk_u8_f32 v7, v11, 1, v10
	v_cvt_pk_u8_f32 v10, v15, 1, v14
	v_cvt_pk_u8_f32 v11, v19, 1, v18
	v_rndne_f32_e32 v9, v9
	v_rndne_f32_e32 v13, v13
	v_rndne_f32_e32 v17, v17
	v_rndne_f32_e32 v5, v5
	v_cvt_pk_u8_f32 v6, v8, 2, v6
	v_cvt_pk_u8_f32 v7, v12, 2, v7
	v_cvt_pk_u8_f32 v8, v16, 2, v10
	v_cvt_pk_u8_f32 v10, v20, 2, v11
	v_cvt_pk_u8_f32 v6, v9, 3, v6
	v_cvt_pk_u8_f32 v7, v13, 3, v7
	v_cvt_pk_u8_f32 v8, v17, 3, v8
	v_cvt_pk_u8_f32 v5, v5, 3, v10
	v_xor_b32_e32 v6, 0x80808080, v6
	v_xor_b32_e32 v7, 0x80808080, v7
	v_xor_b32_e32 v8, 0x80808080, v8
	v_xor_b32_e32 v9, 0x80808080, v5
	v_lshl_add_u64 v[10:11], v[2:3], 0, v[24:25]
	global_store_dwordx4 v[10:11], v[6:9], off nt
.LBB0_877:
	s_or_b64 exec, exec, s[2:3]
	v_or_b32_e32 v5, s18, v74
	v_cmp_gt_i32_e32 vcc, s15, v5
	s_and_saveexec_b64 s[2:3], vcc
	s_cbranch_execz .LBB0_838
	s_lshl_b32 s4, s17, 6
	s_and_b32 s4, s4, 0xffffff00
	v_and_b32_e32 v5, 0x7f, v5
	v_or_b32_e32 v5, s4, v5
	v_or_b32_e32 v6, 0x80, v5
	v_cndmask_b32_e64 v6, v5, v6, s[6:7]
	v_ashrrev_i32_e32 v7, 31, v6
	v_lshl_add_u64 v[8:9], v[6:7], 2, s[0:1]
	v_mov_b32_e32 v24, v179
	v_lshlrev_b64 v[22:23], 11, v[6:7]
	ds_read2_b32 v[8:9], v75 offset0:24 offset1:57
	ds_read2_b32 v[10:11], v75 offset0:90 offset1:123
	ds_read2_b32 v[12:13], v75 offset0:156 offset1:189
	ds_read2_b32 v[14:15], v75 offset0:222 offset1:255
	ds_read2_b32 v[16:17], v4 offset0:32 offset1:65
	ds_read2_b32 v[18:19], v4 offset0:98 offset1:131
	ds_read2_b32 v[4:5], v4 offset0:164 offset1:197
	v_add_u32_e32 v20, 0x600, v75
	ds_read2_b32 v[20:21], v20 offset0:102 offset1:135
	v_lshl_add_u64 v[2:3], v[2:3], 0, v[22:23]
	s_nop 0
	v_div_scale_f32 v25, s[4:5], v24, v24, 1.0
	v_rcp_f32_e32 v26, v25
	v_div_scale_f32 v6, vcc, 1.0, v24, 1.0
	v_fma_f32 v7, -v25, v26, 1.0
	v_fmac_f32_e32 v26, v7, v26
	v_mul_f32_e32 v7, v6, v26
	v_fma_f32 v27, -v25, v7, v6
	v_fmac_f32_e32 v7, v27, v26
	v_fma_f32 v6, -v25, v7, v6
	v_div_fmas_f32 v6, v6, v26, v7
	v_div_fixup_f32 v6, v6, v24, 1.0
	s_waitcnt lgkmcnt(7)
	v_fmaak_f32 v7, v8, v6, 0x43000000
	v_fmaak_f32 v8, v6, v9, 0x43000000
	s_waitcnt lgkmcnt(6)
	v_fmaak_f32 v9, v6, v10, 0x43000000
	v_fmaak_f32 v10, v6, v11, 0x43000000
	s_waitcnt lgkmcnt(5)
	v_fmaak_f32 v11, v6, v12, 0x43000000
	v_fmaak_f32 v12, v6, v13, 0x43000000
	s_waitcnt lgkmcnt(4)
	v_fmaak_f32 v13, v6, v14, 0x43000000
	v_fmaak_f32 v14, v6, v15, 0x43000000
	s_waitcnt lgkmcnt(3)
	v_fmaak_f32 v15, v6, v16, 0x43000000
	s_waitcnt lgkmcnt(1)
	v_fmaak_f32 v4, v6, v4, 0x43000000
	v_fmaak_f32 v16, v6, v17, 0x43000000
	v_fmaak_f32 v5, v6, v5, 0x43000000
	v_rndne_f32_e32 v7, v7
	v_rndne_f32_e32 v11, v11
	v_rndne_f32_e32 v15, v15
	v_rndne_f32_e32 v4, v4
	v_fmaak_f32 v17, v6, v18, 0x43000000
	v_fmaak_f32 v18, v6, v19, 0x43000000
	s_waitcnt lgkmcnt(0)
	v_fmaak_f32 v19, v6, v20, 0x43000000
	v_rndne_f32_e32 v8, v8
	v_rndne_f32_e32 v12, v12
	v_rndne_f32_e32 v16, v16
	v_rndne_f32_e32 v5, v5
	v_cvt_pk_u8_f32 v7, v7, 0, 0
	v_cvt_pk_u8_f32 v11, v11, 0, 0
	v_cvt_pk_u8_f32 v15, v15, 0, 0
	v_cvt_pk_u8_f32 v4, v4, 0, 0
	v_fmaak_f32 v6, v6, v21, 0x43000000
	v_rndne_f32_e32 v9, v9
	v_rndne_f32_e32 v13, v13
	v_rndne_f32_e32 v17, v17
	v_rndne_f32_e32 v19, v19
	v_cvt_pk_u8_f32 v7, v8, 1, v7
	v_cvt_pk_u8_f32 v8, v12, 1, v11
	v_cvt_pk_u8_f32 v11, v16, 1, v15
	v_cvt_pk_u8_f32 v4, v5, 1, v4
	v_rndne_f32_e32 v10, v10
	v_rndne_f32_e32 v14, v14
	v_rndne_f32_e32 v18, v18
	v_rndne_f32_e32 v6, v6
	v_cvt_pk_u8_f32 v5, v9, 2, v7
	v_cvt_pk_u8_f32 v7, v13, 2, v8
	v_cvt_pk_u8_f32 v8, v17, 2, v11
	v_cvt_pk_u8_f32 v4, v19, 2, v4
	v_cvt_pk_u8_f32 v5, v10, 3, v5
	v_cvt_pk_u8_f32 v7, v14, 3, v7
	v_cvt_pk_u8_f32 v8, v18, 3, v8
	v_cvt_pk_u8_f32 v9, v6, 3, v4
	v_xor_b32_e32 v4, 0x80808080, v5
	v_xor_b32_e32 v5, 0x80808080, v7
	v_xor_b32_e32 v6, 0x80808080, v8
	v_xor_b32_e32 v7, 0x80808080, v9
	global_store_dwordx4 v[2:3], v[4:7], off nt
	s_branch .LBB0_838
